# baseline (speedup 1.0000x reference)
.LBB0_2:
	s_or_b64 exec, exec, s[4:5]
	s_load_dwordx2 s[10:11], s[0:1], 0x58
	s_load_dwordx2 s[44:45], s[0:1], 0x20
	s_load_dwordx2 s[68:69], s[0:1], 0x10
	s_movk_i32 s3, 0x160
	v_cmp_gt_u32_e32 vcc, s3, v0
	s_and_saveexec_b64 s[4:5], vcc
	s_cbranch_execz .LBB0_4
	global_load_dword v11, v[2:3], off
.LBB0_4:
	s_or_b64 exec, exec, s[4:5]
	s_lshl_b32 s46, s30, 11
	s_lshl_b32 s3, s2, 10
	s_ashr_i32 s47, s46, 31
	s_and_b32 s33, s3, 0x400
	s_lshl_b64 s[4:5], s[46:47], 2
	s_add_u32 s3, s26, s4
	v_lshlrev_b32_e32 v46, 2, v0
	v_mov_b32_e32 v47, 0
	s_addc_u32 s4, s27, s5
	s_lshl_b32 s5, s33, 2
	s_add_u32 s26, s3, s5
	s_addc_u32 s27, s4, 0
	v_lshlrev_b32_e32 v212, 1, v0
	v_mov_b32_e32 v213, v47
	v_lshl_add_u64 v[32:33], v[212:213], 2, s[26:27]
	v_lshrrev_b32_e32 v219, 6, v0
	v_bfe_u32 v214, v0, 5, 1
	v_and_b32_e32 v220, 31, v0
	s_or_b32 s3, s46, s33
	v_lshlrev_b32_e32 v216, 4, v219
	v_lshlrev_b32_e32 v221, 3, v214
	v_or3_b32 v1, s3, v216, v221
	v_lshlrev_b32_e32 v232, 4, v220
	v_and_b32_e32 v218, 63, v0
	s_mov_b32 s39, 0x20000
	s_brev_b32 s38, 16
	s_and_b32 s37, s37, 0xffff
	v_lshl_or_b32 v180, v1, 9, v232
	v_add_u32_e32 v1, 0x10000, v180
	s_waitcnt lgkmcnt(0)
	global_load_dword v250, v10, s[68:69]
	global_load_dword v251, v10, s[44:45]
	global_load_dwordx2 v[32:33], v[32:33], off
	buffer_load_dwordx4 v[34:37], v180, s[36:39], 0 offen nt
	buffer_load_dwordx4 v[38:41], v180, s[36:39], 0 offen offset:512 nt
	buffer_load_dwordx4 v[42:45], v180, s[36:39], 0 offen offset:1024 nt
	buffer_load_dwordx4 v[96:99], v180, s[36:39], 0 offen offset:1536 nt
	buffer_load_dwordx4 v[100:103], v180, s[36:39], 0 offen offset:2048 nt
	buffer_load_dwordx4 v[104:107], v180, s[36:39], 0 offen offset:2560 nt
	buffer_load_dwordx4 v[108:111], v180, s[36:39], 0 offen offset:3072 nt
	buffer_load_dwordx4 v[112:115], v180, s[36:39], 0 offen offset:3584 nt
	buffer_load_dwordx4 v[116:119], v1, s[36:39], 0 offen nt
	buffer_load_dwordx4 v[120:123], v1, s[36:39], 0 offen offset:512 nt
	buffer_load_dwordx4 v[124:127], v1, s[36:39], 0 offen offset:1024 nt
	buffer_load_dwordx4 v[128:131], v1, s[36:39], 0 offen offset:1536 nt
	buffer_load_dwordx4 v[132:135], v1, s[36:39], 0 offen offset:2048 nt
	buffer_load_dwordx4 v[136:139], v1, s[36:39], 0 offen offset:2560 nt
	buffer_load_dwordx4 v[140:143], v1, s[36:39], 0 offen offset:3072 nt
	buffer_load_dwordx4 v[144:147], v1, s[36:39], 0 offen offset:3584 nt
	s_mov_b32 s3, 0x10000
	v_lshrrev_b32_e32 v227, 5, v0
	v_and_b32_e32 v228, 0x7c, v46
	v_add_u32_e32 v2, 0x200, v0
	v_lshrrev_b32_e32 v229, 5, v2
	v_mul_u32_u24_e32 v246, 0x110, v227
	v_lshl_add_u32 v246, v220, 3, v246
	v_add_u32_e32 v246, 0x10000, v246
	v_lshlrev_b32_e32 v247, 2, v46
	s_waitcnt vmcnt(16)
	v_cmp_ne_u32_e64 s[6:7], 0, v32
	v_cmp_ne_u32_e64 s[4:5], 0, v33
	v_cmp_eq_u32_e64 s[8:9], 0, v218
	s_nop 0
	s_and_saveexec_b64 s[12:13], s[8:9]
	s_cbranch_execz .LBB0_6
	s_bcnt1_i32_b64 s6, s[6:7]
	s_bcnt1_i32_b64 s4, s[4:5]
	v_mov_b32_e32 v1, 0x21100
	s_add_i32 s4, s4, s6
	v_lshl_add_u32 v1, v219, 2, v1
	v_mov_b32_e32 v2, s4
	ds_write_b32 v1, v2
.LBB0_6:
	s_or_b64 exec, exec, s[12:13]
	v_lshrrev_b32_e32 v222, 7, v0
	v_lshlrev_b32_e32 v215, 5, v222
	v_or_b32_e32 v231, v215, v220
	v_mul_u32_u24_e32 v224, 0x110, v231
	v_lshlrev_b32_e32 v223, 1, v221
	v_bfe_u32 v225, v0, 6, 1
	v_add3_u32 v248, v224, v223, s3
	s_waitcnt lgkmcnt(0)
	s_barrier
	s_movk_i32 s4, 0x110
	v_lshlrev_b32_e32 v230, 7, v225
	v_mad_u32_u24 v249, v231, s4, v230
	v_or_b32_e32 v249, v249, v221
	v_add_u32_e32 v249, 0x18800, v249
	v_mov_b32_e32 v1, 0x21100
	v_mov_b32_e32 v2, 0x21110
	ds_read_b128 v[6:9], v1
	ds_read_b128 v[2:5], v2
	s_mul_i32 s4, s2, 0x4590
	s_mul_hi_i32 s3, s2, 0x4590
	s_add_u32 s34, s10, s4
	s_addc_u32 s35, s11, s3
	s_and_saveexec_b64 s[4:5], vcc
	s_cbranch_execz .LBB0_8
	v_mov_b32_e32 v1, 0
	v_lshl_add_u64 v[12:13], v[0:1], 2, s[34:35]
	v_add_co_u32_e32 v12, vcc, 0x4000, v12
	s_nop 1
	v_addc_co_u32_e32 v13, vcc, 0, v13, vcc
	global_store_dword v[12:13], v11, off offset:16

.LBB0_11:
	s_add_i32 s3, s3, 2
	s_cmp_gt_u32 s3, 5
	s_cselect_b64 vcc, -1, 0
	v_add_u32_e32 v184, 0xffff0000, v183
	s_and_b64 s[12:13], vcc, exec
	v_cndmask_b32_e32 v200, v184, v1, vcc
	s_cselect_b32 s15, 0x20000, 0x20000
	s_cselect_b32 s14, 0x10000, s16
	s_cselect_b32 s13, s41, s37
	s_cselect_b32 s12, s22, s36
	s_waitcnt vmcnt(8)
	v_cvt_pk_f16_f32 v187, v172, v176
	v_cvt_pk_f16_f32 v186, v160, v168
	v_cvt_pk_f16_f32 v185, v164, v156
	v_cvt_pk_f16_f32 v184, v148, v152
	v_cvt_pk_f16_f32 v191, v173, v177
	v_cvt_pk_f16_f32 v190, v161, v169
	v_cvt_pk_f16_f32 v189, v165, v157
	v_cvt_pk_f16_f32 v188, v149, v153
	v_cvt_pk_f16_f32 v195, v174, v178
	v_cvt_pk_f16_f32 v194, v162, v170
	v_cvt_pk_f16_f32 v193, v166, v158
	v_cvt_pk_f16_f32 v192, v150, v154
	v_cvt_pk_f16_f32 v199, v175, v179
	v_cvt_pk_f16_f32 v198, v163, v171
	v_cvt_pk_f16_f32 v197, v167, v159
	v_cvt_pk_f16_f32 v196, v151, v155
	buffer_load_dwordx4 v[148:151], v200, s[12:15], 0 offen nt
	buffer_load_dwordx4 v[152:155], v200, s[12:15], 0 offen offset:512 nt
	buffer_load_dwordx4 v[164:167], v200, s[12:15], 0 offen offset:1024 nt
	buffer_load_dwordx4 v[156:159], v200, s[12:15], 0 offen offset:1536 nt
	buffer_load_dwordx4 v[160:163], v200, s[12:15], 0 offen offset:2048 nt
	buffer_load_dwordx4 v[168:171], v200, s[12:15], 0 offen offset:2560 nt
	buffer_load_dwordx4 v[172:175], v200, s[12:15], 0 offen offset:3072 nt
	buffer_load_dwordx4 v[176:179], v200, s[12:15], 0 offen offset:3584 nt
	ds_write_b128 v180, v[184:187]
	ds_write_b128 v180, v[188:191] offset:1024
	ds_write_b128 v180, v[192:195] offset:2048
	ds_write_b128 v180, v[196:199] offset:3072
	s_cselect_b32 s14, s17, 0x8000000
	s_cselect_b32 s13, s29, s37
	s_cselect_b32 s12, s28, s36
	v_cndmask_b32_e32 v200, v183, v1, vcc
	s_cmp_lg_u32 s3, 0
	s_cbranch_scc1 .Lw47_not0
	global_load_dwordx4 v[48:51], v247, s[68:69]
	global_load_dwordx4 v[80:83], v247, s[44:45]
	v_add_u32_e32 v247, 0x2000, v247
	global_load_dwordx4 v[52:55], v247, s[68:69]
	global_load_dwordx4 v[84:87], v247, s[44:45]
	v_add_u32_e32 v247, 0x2000, v247
	global_load_dwordx4 v[56:59], v247, s[68:69]
	global_load_dwordx4 v[88:91], v247, s[44:45]
	v_add_u32_e32 v247, 0x2000, v247
	global_load_dwordx4 v[60:63], v247, s[68:69]
	global_load_dwordx4 v[92:95], v247, s[44:45]
	v_add_u32_e32 v247, 0x2000, v247
	global_load_dwordx4 v[64:67], v247, s[68:69]
	global_load_dwordx4 v[96:99], v247, s[44:45]
	v_add_u32_e32 v247, 0x2000, v247
	global_load_dwordx4 v[68:71], v247, s[68:69]
	global_load_dwordx4 v[100:103], v247, s[44:45]
	v_add_u32_e32 v247, 0x2000, v247
	global_load_dwordx4 v[72:75], v247, s[68:69]
	global_load_dwordx4 v[104:107], v247, s[44:45]
	v_add_u32_e32 v247, 0x2000, v247
	global_load_dwordx4 v[76:79], v247, s[68:69]
	global_load_dwordx4 v[108:111], v247, s[44:45]
	s_branch .Lw47_xdone
.Lw47_not0:
	s_cmp_lg_u32 s3, 2
	s_cbranch_scc1 .Lw47_xdone
	v_cvt_pk_f16_f32 v48, v48, v49
	v_cvt_pk_f16_f32 v49, v50, v51
	ds_write_b64 v246, v[48:49]
	v_cvt_pk_f16_f32 v80, v80, v81
	v_cvt_pk_f16_f32 v81, v82, v83
	ds_write_b64 v246, v[80:81] offset:34816
	v_cvt_pk_f16_f32 v52, v52, v53
	v_cvt_pk_f16_f32 v53, v54, v55
	ds_write_b64 v246, v[52:53] offset:4352
	v_cvt_pk_f16_f32 v84, v84, v85
	v_cvt_pk_f16_f32 v85, v86, v87
	ds_write_b64 v246, v[84:85] offset:39168
	v_cvt_pk_f16_f32 v56, v56, v57
	v_cvt_pk_f16_f32 v57, v58, v59
	ds_write_b64 v246, v[56:57] offset:8704
	v_cvt_pk_f16_f32 v88, v88, v89
	v_cvt_pk_f16_f32 v89, v90, v91
	ds_write_b64 v246, v[88:89] offset:43520
	v_cvt_pk_f16_f32 v60, v60, v61
	v_cvt_pk_f16_f32 v61, v62, v63
	ds_write_b64 v246, v[60:61] offset:13056
	v_cvt_pk_f16_f32 v92, v92, v93
	v_cvt_pk_f16_f32 v93, v94, v95
	ds_write_b64 v246, v[92:93] offset:47872
	v_cvt_pk_f16_f32 v64, v64, v65
	v_cvt_pk_f16_f32 v65, v66, v67
	ds_write_b64 v246, v[64:65] offset:17408
	v_cvt_pk_f16_f32 v96, v96, v97
	v_cvt_pk_f16_f32 v97, v98, v99
	ds_write_b64 v246, v[96:97] offset:52224
	v_cvt_pk_f16_f32 v68, v68, v69
	v_cvt_pk_f16_f32 v69, v70, v71
	ds_write_b64 v246, v[68:69] offset:21760
	v_cvt_pk_f16_f32 v100, v100, v101
	v_cvt_pk_f16_f32 v101, v102, v103
	ds_write_b64 v246, v[100:101] offset:56576
	v_cvt_pk_f16_f32 v72, v72, v73
	v_cvt_pk_f16_f32 v73, v74, v75
	ds_write_b64 v246, v[72:73] offset:26112
	v_cvt_pk_f16_f32 v104, v104, v105
	v_cvt_pk_f16_f32 v105, v106, v107
	ds_write_b64 v246, v[104:105] offset:60928
	v_cvt_pk_f16_f32 v76, v76, v77
	v_cvt_pk_f16_f32 v77, v78, v79
	ds_write_b64 v246, v[76:77] offset:30464
	v_cvt_pk_f16_f32 v108, v108, v109
	v_cvt_pk_f16_f32 v109, v110, v111
	ds_write_b64 v246, v[108:109] offset:65280
.Lw47_xdone:
	s_waitcnt lgkmcnt(0)
	s_barrier
	s_cmp_lg_u32 s3, 2
	s_cbranch_scc1 .Lw47_ydone
	ds_read_b128 v[92:95], v248
	ds_read_b128 v[88:91], v248 offset:32
	ds_read_b128 v[84:87], v248 offset:64
	ds_read_b128 v[80:83], v248 offset:96
	ds_read_b128 v[76:79], v248 offset:128
	ds_read_b128 v[72:75], v248 offset:160
	ds_read_b128 v[68:71], v248 offset:192
	ds_read_b128 v[64:67], v248 offset:224
	ds_read2_b64 v[60:63], v249 offset1:2
	ds_read2_b64 v[56:59], v249 offset0:4 offset1:6
	ds_read2_b64 v[52:55], v249 offset0:8 offset1:10
	ds_read2_b64 v[48:51], v249 offset0:12 offset1:14
	s_waitcnt lgkmcnt(0)
.Lw47_ydone:
	ds_read_b128 v[184:187], v181
	ds_read_b128 v[188:191], v182
	ds_read_b128 v[192:195], v182 offset:1024
	ds_read_b128 v[196:199], v181 offset:4096
	s_waitcnt lgkmcnt(2)
	v_mfma_f32_32x32x16_f16 v[18:33], v[184:187], v[188:191], v[18:33]
	s_waitcnt lgkmcnt(1)
	v_mfma_f32_32x32x16_f16 v[2:17], v[184:187], v[192:195], v[2:17]
	ds_read_b128 v[184:187], v182 offset:4096
	ds_read_b128 v[188:191], v182 offset:5120
	s_waitcnt lgkmcnt(1)
	v_mfma_f32_32x32x16_f16 v[18:33], v[196:199], v[184:187], v[18:33]
	s_waitcnt lgkmcnt(0)
	v_mfma_f32_32x32x16_f16 v[2:17], v[196:199], v[188:191], v[2:17]
	ds_read_b128 v[184:187], v181 offset:8192
	ds_read_b128 v[188:191], v182 offset:8192
	ds_read_b128 v[192:195], v182 offset:9216
	ds_read_b128 v[196:199], v181 offset:12288
	s_waitcnt lgkmcnt(2)
	v_mfma_f32_32x32x16_f16 v[18:33], v[184:187], v[188:191], v[18:33]
	s_waitcnt lgkmcnt(1)
	v_mfma_f32_32x32x16_f16 v[2:17], v[184:187], v[192:195], v[2:17]
	ds_read_b128 v[184:187], v182 offset:12288
	ds_read_b128 v[188:191], v182 offset:13312
	s_waitcnt lgkmcnt(1)
	v_mfma_f32_32x32x16_f16 v[18:33], v[196:199], v[184:187], v[18:33]
	s_waitcnt lgkmcnt(0)
	v_mfma_f32_32x32x16_f16 v[2:17], v[196:199], v[188:191], v[2:17]
	ds_read_b128 v[184:187], v181 offset:16384
	ds_read_b128 v[188:191], v182 offset:16384
	ds_read_b128 v[192:195], v182 offset:17408
	ds_read_b128 v[196:199], v181 offset:20480
	s_waitcnt lgkmcnt(2)
	v_mfma_f32_32x32x16_f16 v[18:33], v[184:187], v[188:191], v[18:33]
	s_waitcnt lgkmcnt(1)
	v_mfma_f32_32x32x16_f16 v[2:17], v[184:187], v[192:195], v[2:17]
	ds_read_b128 v[184:187], v182 offset:20480
	ds_read_b128 v[188:191], v182 offset:21504
	s_waitcnt lgkmcnt(1)
	v_mfma_f32_32x32x16_f16 v[18:33], v[196:199], v[184:187], v[18:33]
	s_waitcnt lgkmcnt(0)
	v_mfma_f32_32x32x16_f16 v[2:17], v[196:199], v[188:191], v[2:17]
	ds_read_b128 v[184:187], v181 offset:24576
	ds_read_b128 v[188:191], v182 offset:24576
	ds_read_b128 v[192:195], v182 offset:25600
	ds_read_b128 v[196:199], v181 offset:28672
	s_waitcnt lgkmcnt(2)
	v_mfma_f32_32x32x16_f16 v[18:33], v[184:187], v[188:191], v[18:33]
	s_waitcnt lgkmcnt(1)
	v_mfma_f32_32x32x16_f16 v[2:17], v[184:187], v[192:195], v[2:17]
	ds_read_b128 v[184:187], v182 offset:28672
	ds_read_b128 v[188:191], v182 offset:29696
	s_waitcnt lgkmcnt(1)
	v_mfma_f32_32x32x16_f16 v[18:33], v[196:199], v[184:187], v[18:33]
	s_waitcnt lgkmcnt(0)
	v_mfma_f32_32x32x16_f16 v[2:17], v[196:199], v[188:191], v[2:17]
	s_cmp_lg_u32 s3, 0
	s_cbranch_scc1 .Lw47_w8
	s_waitcnt vmcnt(24)
	s_branch .Lw47_wdone
.Lw47_w8:
	s_waitcnt vmcnt(8)
.Lw47_wdone:
	v_cvt_pk_f16_f32 v187, v140, v144
	v_cvt_pk_f16_f32 v186, v132, v136
	v_cvt_pk_f16_f32 v185, v124, v128
	v_cvt_pk_f16_f32 v184, v116, v120
	v_cvt_pk_f16_f32 v191, v141, v145
	v_cvt_pk_f16_f32 v190, v133, v137
	v_cvt_pk_f16_f32 v189, v125, v129
	v_cvt_pk_f16_f32 v188, v117, v121
	v_cvt_pk_f16_f32 v195, v142, v146
	v_cvt_pk_f16_f32 v194, v134, v138
	v_cvt_pk_f16_f32 v193, v126, v130
	v_cvt_pk_f16_f32 v192, v118, v122
	v_cvt_pk_f16_f32 v199, v143, v147
	v_cvt_pk_f16_f32 v198, v135, v139
	v_cvt_pk_f16_f32 v197, v127, v131
	v_cvt_pk_f16_f32 v196, v119, v123
	buffer_load_dwordx4 v[116:119], v200, s[12:15], 0 offen nt
	buffer_load_dwordx4 v[120:123], v200, s[12:15], 0 offen offset:512 nt
	buffer_load_dwordx4 v[124:127], v200, s[12:15], 0 offen offset:1024 nt
	buffer_load_dwordx4 v[128:131], v200, s[12:15], 0 offen offset:1536 nt
	buffer_load_dwordx4 v[132:135], v200, s[12:15], 0 offen offset:2048 nt
	buffer_load_dwordx4 v[136:139], v200, s[12:15], 0 offen offset:2560 nt
	buffer_load_dwordx4 v[140:143], v200, s[12:15], 0 offen offset:3072 nt
	buffer_load_dwordx4 v[144:147], v200, s[12:15], 0 offen offset:3584 nt
	ds_write_b128 v180, v[184:187] offset:32768
	ds_write_b128 v180, v[188:191] offset:33792
	ds_write_b128 v180, v[192:195] offset:34816
	ds_write_b128 v180, v[196:199] offset:35840
	s_waitcnt lgkmcnt(0)
	s_barrier
	ds_read_b128 v[184:187], v181 offset:32768
	ds_read_b128 v[188:191], v182 offset:32768
	ds_read_b128 v[192:195], v182 offset:33792
	ds_read_b128 v[196:199], v181 offset:36864
	s_waitcnt lgkmcnt(2)
	v_mfma_f32_32x32x16_f16 v[18:33], v[184:187], v[188:191], v[18:33]
	v_add_u32_e32 v183, 0x20000, v183
	s_cmp_lt_u32 s3, 6
	s_waitcnt lgkmcnt(1)
	v_mfma_f32_32x32x16_f16 v[2:17], v[184:187], v[192:195], v[2:17]
	ds_read_b128 v[184:187], v182 offset:36864
	ds_read_b128 v[188:191], v182 offset:37888
	s_waitcnt lgkmcnt(1)
	v_mfma_f32_32x32x16_f16 v[18:33], v[196:199], v[184:187], v[18:33]
	s_waitcnt lgkmcnt(0)
	v_mfma_f32_32x32x16_f16 v[2:17], v[196:199], v[188:191], v[2:17]
	ds_read_b128 v[184:187], v181 offset:40960
	ds_read_b128 v[188:191], v182 offset:40960
	ds_read_b128 v[192:195], v182 offset:41984
	ds_read_b128 v[196:199], v181 offset:45056
	s_waitcnt lgkmcnt(2)
	v_mfma_f32_32x32x16_f16 v[18:33], v[184:187], v[188:191], v[18:33]
	s_waitcnt lgkmcnt(1)
	v_mfma_f32_32x32x16_f16 v[2:17], v[184:187], v[192:195], v[2:17]
	ds_read_b128 v[184:187], v182 offset:45056
	ds_read_b128 v[188:191], v182 offset:46080
	s_waitcnt lgkmcnt(1)
	v_mfma_f32_32x32x16_f16 v[18:33], v[196:199], v[184:187], v[18:33]
	s_waitcnt lgkmcnt(0)
	v_mfma_f32_32x32x16_f16 v[2:17], v[196:199], v[188:191], v[2:17]
	ds_read_b128 v[184:187], v181 offset:49152
	ds_read_b128 v[188:191], v182 offset:49152
	ds_read_b128 v[192:195], v182 offset:50176
	ds_read_b128 v[196:199], v181 offset:53248
	s_waitcnt lgkmcnt(2)
	v_mfma_f32_32x32x16_f16 v[18:33], v[184:187], v[188:191], v[18:33]
	s_waitcnt lgkmcnt(1)
	v_mfma_f32_32x32x16_f16 v[2:17], v[184:187], v[192:195], v[2:17]
	ds_read_b128 v[184:187], v182 offset:53248
	ds_read_b128 v[188:191], v182 offset:54272
	s_waitcnt lgkmcnt(1)
	v_mfma_f32_32x32x16_f16 v[18:33], v[196:199], v[184:187], v[18:33]
	s_waitcnt lgkmcnt(0)
	v_mfma_f32_32x32x16_f16 v[2:17], v[196:199], v[188:191], v[2:17]
	ds_read_b128 v[184:187], v181 offset:57344
	ds_read_b128 v[188:191], v182 offset:57344
	ds_read_b128 v[192:195], v182 offset:58368
	ds_read_b128 v[196:199], v181 offset:61440
	s_waitcnt lgkmcnt(2)
	v_mfma_f32_32x32x16_f16 v[18:33], v[184:187], v[188:191], v[18:33]
	s_waitcnt lgkmcnt(1)
	v_mfma_f32_32x32x16_f16 v[2:17], v[184:187], v[192:195], v[2:17]
	ds_read_b128 v[184:187], v182 offset:61440
	ds_read_b128 v[188:191], v182 offset:62464
	s_waitcnt lgkmcnt(1)
	v_mfma_f32_32x32x16_f16 v[18:33], v[196:199], v[184:187], v[18:33]
	s_waitcnt lgkmcnt(0)
	v_mfma_f32_32x32x16_f16 v[2:17], v[196:199], v[188:191], v[2:17]
	s_cbranch_scc1 .LBB0_11
.LBB0_13:
	s_or_saveexec_b64 s[10:11], s[10:11]
	v_mov_b32_e32 v217, 0
	s_xor_b64 exec, exec, s[10:11]
	s_cbranch_execz .LBB0_19
	s_nop 6
	v_add_u32_e32 v2, 0x20000, v180
	buffer_load_dwordx4 v[148:151], v2, s[36:39], 0 offen nt
	buffer_load_dwordx4 v[152:155], v2, s[36:39], 0 offen offset:512 nt
	buffer_load_dwordx4 v[164:167], v2, s[36:39], 0 offen offset:1024 nt
	buffer_load_dwordx4 v[156:159], v2, s[36:39], 0 offen offset:1536 nt
	buffer_load_dwordx4 v[160:163], v2, s[36:39], 0 offen offset:2048 nt
	buffer_load_dwordx4 v[168:171], v2, s[36:39], 0 offen offset:2560 nt
	buffer_load_dwordx4 v[172:175], v2, s[36:39], 0 offen offset:3072 nt
	buffer_load_dwordx4 v[176:179], v2, s[36:39], 0 offen offset:3584 nt
	v_lshlrev_b32_e32 v233, 4, v218
	s_waitcnt vmcnt(16)
	v_cvt_pk_f16_f32 v5, v108, v112
	v_cvt_pk_f16_f32 v4, v100, v104
	v_cvt_pk_f16_f32 v3, v42, v96
	v_cvt_pk_f16_f32 v2, v34, v38
	v_lshl_or_b32 v234, v219, 12, v233
	ds_write_b128 v234, v[2:5]
	v_cvt_pk_f16_f32 v5, v109, v113
	v_cvt_pk_f16_f32 v4, v101, v105
	v_cvt_pk_f16_f32 v3, v43, v97
	v_cvt_pk_f16_f32 v2, v35, v39
	ds_write_b128 v234, v[2:5] offset:1024
	v_cvt_pk_f16_f32 v5, v110, v114
	v_cvt_pk_f16_f32 v4, v102, v106
	v_cvt_pk_f16_f32 v3, v44, v98
	v_cvt_pk_f16_f32 v2, v36, v40
	s_movk_i32 s12, 0xf400
	ds_write_b128 v234, v[2:5] offset:2048
	v_cvt_pk_f16_f32 v5, v111, v115
	v_cvt_pk_f16_f32 v4, v103, v107
	v_cvt_pk_f16_f32 v3, v45, v99
	v_cvt_pk_f16_f32 v2, v37, v41
	v_mad_i32_i24 v235, v219, s12, v234
	s_add_i32 s12, s46, s33
	ds_write_b128 v234, v[2:5] offset:3072
	global_load_dwordx4 v[48:51], v247, s[68:69]
	global_load_dwordx4 v[80:83], v247, s[44:45]
	v_add_u32_e32 v247, 0x2000, v247
	global_load_dwordx4 v[52:55], v247, s[68:69]
	global_load_dwordx4 v[84:87], v247, s[44:45]
	v_add_u32_e32 v247, 0x2000, v247
	global_load_dwordx4 v[56:59], v247, s[68:69]
	global_load_dwordx4 v[88:91], v247, s[44:45]
	v_add_u32_e32 v247, 0x2000, v247
	global_load_dwordx4 v[60:63], v247, s[68:69]
	global_load_dwordx4 v[92:95], v247, s[44:45]
	v_add_u32_e32 v247, 0x2000, v247
	global_load_dwordx4 v[64:67], v247, s[68:69]
	global_load_dwordx4 v[96:99], v247, s[44:45]
	v_add_u32_e32 v247, 0x2000, v247
	global_load_dwordx4 v[68:71], v247, s[68:69]
	global_load_dwordx4 v[100:103], v247, s[44:45]
	v_add_u32_e32 v247, 0x2000, v247
	global_load_dwordx4 v[72:75], v247, s[68:69]
	global_load_dwordx4 v[104:107], v247, s[44:45]
	v_add_u32_e32 v247, 0x2000, v247
	global_load_dwordx4 v[76:79], v247, s[68:69]
	global_load_dwordx4 v[108:111], v247, s[44:45]
	v_add3_u32 v2, s12, v216, v221
	v_lshl_or_b32 v2, v2, 9, v232
	v_mov_b32_e32 v217, 0
	s_mov_b32 s3, 0
	v_add_u32_e32 v236, 0x40000, v2
	s_mov_b32 s16, 0x10000
	v_mov_b32_e32 v2, v217
	v_mov_b32_e32 v3, v217
	v_mov_b32_e32 v4, v217
	v_mov_b32_e32 v5, v217
	v_mov_b32_e32 v6, v217
	v_mov_b32_e32 v7, v217
	v_mov_b32_e32 v8, v217
	v_mov_b32_e32 v9, v217
	v_mov_b32_e32 v10, v217
	v_mov_b32_e32 v11, v217
	v_mov_b32_e32 v12, v217
	v_mov_b32_e32 v13, v217
	v_mov_b32_e32 v14, v217
	v_mov_b32_e32 v15, v217
	v_mov_b32_e32 v16, v217
	v_mov_b32_e32 v17, v217
	v_mov_b32_e32 v18, v217
	v_mov_b32_e32 v19, v217
	v_mov_b32_e32 v20, v217
	v_mov_b32_e32 v21, v217
	v_mov_b32_e32 v22, v217
	v_mov_b32_e32 v23, v217
	v_mov_b32_e32 v24, v217
	v_mov_b32_e32 v25, v217
	v_mov_b32_e32 v26, v217
	v_mov_b32_e32 v27, v217
	v_mov_b32_e32 v28, v217
	v_mov_b32_e32 v29, v217
	v_mov_b32_e32 v30, v217
	v_mov_b32_e32 v31, v217
	v_mov_b32_e32 v32, v217
	v_mov_b32_e32 v33, v217
	s_branch .LBB0_16

.LBB0_16:
	s_cmp_gt_u32 s3, 4
	s_cselect_b64 vcc, -1, 0
	v_add_u32_e32 v180, 0xffff0000, v236
	s_and_b64 s[12:13], vcc, exec
	v_cndmask_b32_e32 v196, v180, v1, vcc
	s_cselect_b32 s13, s29, s37
	s_cselect_b32 s12, s28, s36
	s_cselect_b32 s15, 0x20000, 0x20000
	s_cselect_b32 s14, s16, 0x8000000
	s_waitcnt lgkmcnt(0)
	s_barrier
	s_cmp_lg_u32 s3, 2
	s_cbranch_scc1 .Lw03_ydone
	ds_read_b128 v[92:95], v248
	ds_read_b128 v[88:91], v248 offset:32
	ds_read_b128 v[84:87], v248 offset:64
	ds_read_b128 v[80:83], v248 offset:96
	ds_read_b128 v[76:79], v248 offset:128
	ds_read_b128 v[72:75], v248 offset:160
	ds_read_b128 v[68:71], v248 offset:192
	ds_read_b128 v[64:67], v248 offset:224
	ds_read2_b64 v[60:63], v249 offset1:2
	ds_read2_b64 v[56:59], v249 offset0:4 offset1:6
	ds_read2_b64 v[52:55], v249 offset0:8 offset1:10
	ds_read2_b64 v[48:51], v249 offset0:12 offset1:14
	s_waitcnt lgkmcnt(0)
.Lw03_ydone:
	s_cmp_lg_u32 s3, 0
	s_cbranch_scc1 .Lw03_w8
	s_waitcnt vmcnt(24)
	s_branch .Lw03_wdone

.Lw03_wdone:
	v_cvt_pk_f16_f32 v183, v140, v144
	v_cvt_pk_f16_f32 v182, v132, v136
	v_cvt_pk_f16_f32 v181, v124, v128
	v_cvt_pk_f16_f32 v180, v116, v120
	v_cvt_pk_f16_f32 v187, v141, v145
	v_cvt_pk_f16_f32 v186, v133, v137
	v_cvt_pk_f16_f32 v185, v125, v129
	v_cvt_pk_f16_f32 v184, v117, v121
	v_cvt_pk_f16_f32 v191, v142, v146
	v_cvt_pk_f16_f32 v190, v134, v138
	v_cvt_pk_f16_f32 v189, v126, v130
	v_cvt_pk_f16_f32 v188, v118, v122
	v_cvt_pk_f16_f32 v195, v143, v147
	v_cvt_pk_f16_f32 v194, v135, v139
	v_cvt_pk_f16_f32 v193, v127, v131
	v_cvt_pk_f16_f32 v192, v119, v123
	buffer_load_dwordx4 v[116:119], v196, s[12:15], 0 offen nt
	buffer_load_dwordx4 v[120:123], v196, s[12:15], 0 offen offset:512 nt
	buffer_load_dwordx4 v[124:127], v196, s[12:15], 0 offen offset:1024 nt
	buffer_load_dwordx4 v[128:131], v196, s[12:15], 0 offen offset:1536 nt
	buffer_load_dwordx4 v[132:135], v196, s[12:15], 0 offen offset:2048 nt
	buffer_load_dwordx4 v[136:139], v196, s[12:15], 0 offen offset:2560 nt
	buffer_load_dwordx4 v[140:143], v196, s[12:15], 0 offen offset:3072 nt
	buffer_load_dwordx4 v[144:147], v196, s[12:15], 0 offen offset:3584 nt
	ds_write_b128 v234, v[180:183] offset:32768
	ds_write_b128 v234, v[184:187] offset:33792
	ds_write_b128 v234, v[188:191] offset:34816
	ds_write_b128 v234, v[192:195] offset:35840
	ds_read_b128 v[180:183], v235
	ds_read_b128 v[188:191], v233
	ds_read_b128 v[192:195], v233 offset:1024
	ds_read_b128 v[184:187], v235 offset:4096
	s_waitcnt lgkmcnt(2)
	v_mfma_f32_32x32x16_f16 v[18:33], v[180:183], v[188:191], v[18:33]
	s_waitcnt lgkmcnt(1)
	v_mfma_f32_32x32x16_f16 v[2:17], v[180:183], v[192:195], v[2:17]
	ds_read_b128 v[188:191], v233 offset:4096
	ds_read_b128 v[192:195], v233 offset:5120
	s_waitcnt lgkmcnt(1)
	v_mfma_f32_32x32x16_f16 v[18:33], v[184:187], v[188:191], v[18:33]
	s_waitcnt lgkmcnt(0)
	v_mfma_f32_32x32x16_f16 v[2:17], v[184:187], v[192:195], v[2:17]
	ds_read_b128 v[188:191], v235 offset:8192
	ds_read_b128 v[196:199], v233 offset:8192
	ds_read_b128 v[200:203], v233 offset:9216
	ds_read_b128 v[192:195], v235 offset:12288
	s_waitcnt lgkmcnt(2)
	v_mfma_f32_32x32x16_f16 v[18:33], v[188:191], v[196:199], v[18:33]
	s_waitcnt lgkmcnt(1)
	v_mfma_f32_32x32x16_f16 v[2:17], v[188:191], v[200:203], v[2:17]
	ds_read_b128 v[196:199], v233 offset:12288
	ds_read_b128 v[200:203], v233 offset:13312
	s_waitcnt lgkmcnt(1)
	v_mfma_f32_32x32x16_f16 v[18:33], v[192:195], v[196:199], v[18:33]
	s_waitcnt lgkmcnt(0)
	v_mfma_f32_32x32x16_f16 v[2:17], v[192:195], v[200:203], v[2:17]
	ds_read_b128 v[196:199], v235 offset:16384
	ds_read_b128 v[204:207], v233 offset:16384
	ds_read_b128 v[208:211], v233 offset:17408
	ds_read_b128 v[200:203], v235 offset:20480
	s_waitcnt lgkmcnt(2)
	v_mfma_f32_32x32x16_f16 v[18:33], v[196:199], v[204:207], v[18:33]
	s_waitcnt lgkmcnt(1)
	v_mfma_f32_32x32x16_f16 v[2:17], v[196:199], v[208:211], v[2:17]
	ds_read_b128 v[204:207], v233 offset:20480
	ds_read_b128 v[208:211], v233 offset:21504
	s_waitcnt lgkmcnt(1)
	v_mfma_f32_32x32x16_f16 v[18:33], v[200:203], v[204:207], v[18:33]
	s_waitcnt lgkmcnt(0)
	v_mfma_f32_32x32x16_f16 v[2:17], v[200:203], v[208:211], v[2:17]
	ds_read_b128 v[204:207], v235 offset:24576
	ds_read_b128 v[238:241], v233 offset:24576
	ds_read_b128 v[242:245], v233 offset:25600
	ds_read_b128 v[208:211], v235 offset:28672
	s_waitcnt lgkmcnt(2)
	v_mfma_f32_32x32x16_f16 v[18:33], v[204:207], v[238:241], v[18:33]
	s_waitcnt lgkmcnt(1)
	v_mfma_f32_32x32x16_f16 v[2:17], v[204:207], v[242:245], v[2:17]
	ds_read_b128 v[238:241], v233 offset:28672
	ds_read_b128 v[242:245], v233 offset:29696
	s_waitcnt lgkmcnt(1)
	v_mfma_f32_32x32x16_f16 v[18:33], v[208:211], v[238:241], v[18:33]
	s_waitcnt lgkmcnt(0)
	v_mfma_f32_32x32x16_f16 v[2:17], v[208:211], v[242:245], v[2:17]
	s_cmp_gt_u32 s3, 5
	s_cselect_b64 s[12:13], -1, 0
	s_and_b64 vcc, exec, s[12:13]
	s_barrier
	s_cbranch_vccnz .LBB0_15
	s_waitcnt vmcnt(8)
	v_cvt_pk_f16_f32 v241, v172, v176
	v_cvt_pk_f16_f32 v240, v160, v168
	v_cvt_pk_f16_f32 v239, v164, v156
	v_cvt_pk_f16_f32 v238, v148, v152
	ds_write_b128 v234, v[238:241]
	v_cvt_pk_f16_f32 v241, v173, v177
	v_cvt_pk_f16_f32 v240, v161, v169
	v_cvt_pk_f16_f32 v239, v165, v157
	v_cvt_pk_f16_f32 v238, v149, v153
	ds_write_b128 v234, v[238:241] offset:1024
	v_cvt_pk_f16_f32 v241, v174, v178
	v_cvt_pk_f16_f32 v240, v162, v170
	v_cvt_pk_f16_f32 v239, v166, v158
	v_cvt_pk_f16_f32 v238, v150, v154
	v_cvt_pk_f16_f32 v161, v175, v179
	v_cvt_pk_f16_f32 v160, v163, v171
	v_cvt_pk_f16_f32 v159, v167, v159
	v_cvt_pk_f16_f32 v158, v151, v155
	ds_write_b128 v234, v[238:241] offset:2048
	ds_write_b128 v234, v[158:161] offset:3072
	s_cmp_lg_u32 s3, 0
	s_cbranch_scc1 .LBB0_15
	v_cvt_pk_f16_f32 v48, v48, v49
	v_cvt_pk_f16_f32 v49, v50, v51
	ds_write_b64 v246, v[48:49]
	v_cvt_pk_f16_f32 v80, v80, v81
	v_cvt_pk_f16_f32 v81, v82, v83
	ds_write_b64 v246, v[80:81] offset:34816
	v_cvt_pk_f16_f32 v52, v52, v53
	v_cvt_pk_f16_f32 v53, v54, v55
	ds_write_b64 v246, v[52:53] offset:4352
	v_cvt_pk_f16_f32 v84, v84, v85
	v_cvt_pk_f16_f32 v85, v86, v87
	ds_write_b64 v246, v[84:85] offset:39168
	v_cvt_pk_f16_f32 v56, v56, v57
	v_cvt_pk_f16_f32 v57, v58, v59
	ds_write_b64 v246, v[56:57] offset:8704
	v_cvt_pk_f16_f32 v88, v88, v89
	v_cvt_pk_f16_f32 v89, v90, v91
	ds_write_b64 v246, v[88:89] offset:43520
	v_cvt_pk_f16_f32 v60, v60, v61
	v_cvt_pk_f16_f32 v61, v62, v63
	ds_write_b64 v246, v[60:61] offset:13056
	v_cvt_pk_f16_f32 v92, v92, v93
	v_cvt_pk_f16_f32 v93, v94, v95
	ds_write_b64 v246, v[92:93] offset:47872
	v_cvt_pk_f16_f32 v64, v64, v65
	v_cvt_pk_f16_f32 v65, v66, v67
	ds_write_b64 v246, v[64:65] offset:17408
	v_cvt_pk_f16_f32 v96, v96, v97
	v_cvt_pk_f16_f32 v97, v98, v99
	ds_write_b64 v246, v[96:97] offset:52224
	v_cvt_pk_f16_f32 v68, v68, v69
	v_cvt_pk_f16_f32 v69, v70, v71
	ds_write_b64 v246, v[68:69] offset:21760
	v_cvt_pk_f16_f32 v100, v100, v101
	v_cvt_pk_f16_f32 v101, v102, v103
	ds_write_b64 v246, v[100:101] offset:56576
	v_cvt_pk_f16_f32 v72, v72, v73
	v_cvt_pk_f16_f32 v73, v74, v75
	ds_write_b64 v246, v[72:73] offset:26112
	v_cvt_pk_f16_f32 v104, v104, v105
	v_cvt_pk_f16_f32 v105, v106, v107
	ds_write_b64 v246, v[104:105] offset:60928
	v_cvt_pk_f16_f32 v76, v76, v77
	v_cvt_pk_f16_f32 v77, v78, v79
	ds_write_b64 v246, v[76:77] offset:30464
	v_cvt_pk_f16_f32 v108, v108, v109
	v_cvt_pk_f16_f32 v109, v110, v111
	ds_write_b64 v246, v[108:109] offset:65280
	s_branch .LBB0_15
.LBB0_18:
	global_load_dwordx4 v[48:51], v247, s[68:69]
	global_load_dwordx4 v[80:83], v247, s[44:45]
	v_add_u32_e32 v247, 0x2000, v247
	global_load_dwordx4 v[52:55], v247, s[68:69]
	global_load_dwordx4 v[84:87], v247, s[44:45]
	v_add_u32_e32 v247, 0x2000, v247
	global_load_dwordx4 v[56:59], v247, s[68:69]
	global_load_dwordx4 v[88:91], v247, s[44:45]
	v_add_u32_e32 v247, 0x2000, v247
	global_load_dwordx4 v[60:63], v247, s[68:69]
	global_load_dwordx4 v[92:95], v247, s[44:45]
	v_add_u32_e32 v247, 0x2000, v247
	global_load_dwordx4 v[64:67], v247, s[68:69]
	global_load_dwordx4 v[2:5], v247, s[44:45]
	v_add_u32_e32 v247, 0x2000, v247
	global_load_dwordx4 v[68:71], v247, s[68:69]
	global_load_dwordx4 v[6:9], v247, s[44:45]
	v_add_u32_e32 v247, 0x2000, v247
	global_load_dwordx4 v[72:75], v247, s[68:69]
	global_load_dwordx4 v[10:13], v247, s[44:45]
	v_add_u32_e32 v247, 0x2000, v247
	global_load_dwordx4 v[76:79], v247, s[68:69]
	global_load_dwordx4 v[14:17], v247, s[44:45]
	s_waitcnt vmcnt(0)
	v_cvt_pk_f16_f32 v48, v48, v49
	v_cvt_pk_f16_f32 v49, v50, v51
	ds_write_b64 v246, v[48:49]
	v_cvt_pk_f16_f32 v80, v80, v81
	v_cvt_pk_f16_f32 v81, v82, v83
	ds_write_b64 v246, v[80:81] offset:34816
	v_cvt_pk_f16_f32 v52, v52, v53
	v_cvt_pk_f16_f32 v53, v54, v55
	ds_write_b64 v246, v[52:53] offset:4352
	v_cvt_pk_f16_f32 v84, v84, v85
	v_cvt_pk_f16_f32 v85, v86, v87
	ds_write_b64 v246, v[84:85] offset:39168
	v_cvt_pk_f16_f32 v56, v56, v57
	v_cvt_pk_f16_f32 v57, v58, v59
	ds_write_b64 v246, v[56:57] offset:8704
	v_cvt_pk_f16_f32 v88, v88, v89
	v_cvt_pk_f16_f32 v89, v90, v91
	ds_write_b64 v246, v[88:89] offset:43520
	v_cvt_pk_f16_f32 v60, v60, v61
	v_cvt_pk_f16_f32 v61, v62, v63
	ds_write_b64 v246, v[60:61] offset:13056
	v_cvt_pk_f16_f32 v92, v92, v93
	v_cvt_pk_f16_f32 v93, v94, v95
	ds_write_b64 v246, v[92:93] offset:47872
	v_cvt_pk_f16_f32 v64, v64, v65
	v_cvt_pk_f16_f32 v65, v66, v67
	ds_write_b64 v246, v[64:65] offset:17408
	v_cvt_pk_f16_f32 v2, v2, v3
	v_cvt_pk_f16_f32 v3, v4, v5
	ds_write_b64 v246, v[2:3] offset:52224
	v_cvt_pk_f16_f32 v68, v68, v69
	v_cvt_pk_f16_f32 v69, v70, v71
	ds_write_b64 v246, v[68:69] offset:21760
	v_cvt_pk_f16_f32 v6, v6, v7
	v_cvt_pk_f16_f32 v7, v8, v9
	ds_write_b64 v246, v[6:7] offset:56576
	v_cvt_pk_f16_f32 v72, v72, v73
	v_cvt_pk_f16_f32 v73, v74, v75
	ds_write_b64 v246, v[72:73] offset:26112
	v_cvt_pk_f16_f32 v10, v10, v11
	v_cvt_pk_f16_f32 v11, v12, v13
	ds_write_b64 v246, v[10:11] offset:60928
	v_cvt_pk_f16_f32 v76, v76, v77
	v_cvt_pk_f16_f32 v77, v78, v79
	ds_write_b64 v246, v[76:77] offset:30464
	v_cvt_pk_f16_f32 v14, v14, v15
	v_cvt_pk_f16_f32 v15, v16, v17
	ds_write_b64 v246, v[14:15] offset:65280
	s_waitcnt lgkmcnt(0)
	s_barrier
	ds_read_b128 v[92:95], v248
	ds_read_b128 v[88:91], v248 offset:32
	ds_read_b128 v[84:87], v248 offset:64
	ds_read_b128 v[80:83], v248 offset:96
	ds_read_b128 v[76:79], v248 offset:128
	ds_read_b128 v[72:75], v248 offset:160
	ds_read_b128 v[68:71], v248 offset:192
	ds_read_b128 v[64:67], v248 offset:224
	ds_read2_b64 v[60:63], v249 offset1:2
	ds_read2_b64 v[56:59], v249 offset0:4 offset1:6
	ds_read2_b64 v[52:55], v249 offset0:8 offset1:10
	ds_read2_b64 v[48:51], v249 offset0:12 offset1:14
	s_waitcnt lgkmcnt(0)
	s_mov_b64 s[10:11], -1
	s_branch .LBB0_20

	.amdhsa_kernel _Z11gram_kernelPKfPKiS0_S0_S0_S0_S0_S0_S0_S0_S0_Pf
		.amdhsa_group_segment_fixed_size 135456
		.amdhsa_private_segment_fixed_size 0
		.amdhsa_kernarg_size 96
		.amdhsa_user_sgpr_count 2
		.amdhsa_user_sgpr_dispatch_ptr 0
		.amdhsa_user_sgpr_queue_ptr 0
		.amdhsa_user_sgpr_kernarg_segment_ptr 1
		.amdhsa_user_sgpr_dispatch_id 0
		.amdhsa_user_sgpr_kernarg_preload_length 0
		.amdhsa_user_sgpr_kernarg_preload_offset 0
		.amdhsa_user_sgpr_private_segment_size 0
		.amdhsa_uses_dynamic_stack 0
		.amdhsa_enable_private_segment 0
		.amdhsa_system_sgpr_workgroup_id_x 1
		.amdhsa_system_sgpr_workgroup_id_y 0
		.amdhsa_system_sgpr_workgroup_id_z 0
		.amdhsa_system_sgpr_workgroup_info 0
		.amdhsa_system_vgpr_workitem_id 0
		.amdhsa_next_free_vgpr 252
		.amdhsa_next_free_sgpr 96
		.amdhsa_accum_offset 252
		.amdhsa_reserve_vcc 1
		.amdhsa_float_round_mode_32 0
		.amdhsa_float_round_mode_16_64 0
		.amdhsa_float_denorm_mode_32 3
		.amdhsa_float_denorm_mode_16_64 3
		.amdhsa_dx10_clamp 1
		.amdhsa_ieee_mode 1
		.amdhsa_fp16_overflow 0
		.amdhsa_tg_split 0
		.amdhsa_exception_fp_ieee_invalid_op 0
		.amdhsa_exception_fp_denorm_src 0
		.amdhsa_exception_fp_ieee_div_zero 0
		.amdhsa_exception_fp_ieee_overflow 0
		.amdhsa_exception_fp_ieee_underflow 0
		.amdhsa_exception_fp_ieee_inexact 0
		.amdhsa_exception_int_div_zero 0
	.end_amdhsa_kernel

amdhsa.kernels:
  - .agpr_count:     0
    .args:
      - .actual_access:  read_only
        .address_space:  global
        .offset:         0
        .size:           8
        .value_kind:     global_buffer
      - .actual_access:  read_only
        .address_space:  global
        .offset:         8
        .size:           8
        .value_kind:     global_buffer
      - .actual_access:  read_only
        .address_space:  global
        .offset:         16
        .size:           8
        .value_kind:     global_buffer
      - .actual_access:  read_only
        .address_space:  global
        .offset:         24
        .size:           8
        .value_kind:     global_buffer
      - .actual_access:  read_only
        .address_space:  global
        .offset:         32
        .size:           8
        .value_kind:     global_buffer
      - .actual_access:  read_only
        .address_space:  global
        .offset:         40
        .size:           8
        .value_kind:     global_buffer
      - .address_space:  global
        .offset:         48
        .size:           8
        .value_kind:     global_buffer
      - .address_space:  global
        .offset:         56
        .size:           8
        .value_kind:     global_buffer
      - .address_space:  global
        .offset:         64
        .size:           8
        .value_kind:     global_buffer
      - .actual_access:  read_only
        .address_space:  global
        .offset:         72
        .size:           8
        .value_kind:     global_buffer
      - .actual_access:  read_only
        .address_space:  global
        .offset:         80
        .size:           8
        .value_kind:     global_buffer
      - .actual_access:  write_only
        .address_space:  global
        .offset:         88
        .size:           8
        .value_kind:     global_buffer
    .group_segment_fixed_size: 135456
    .kernarg_segment_align: 8
    .kernarg_segment_size: 96
    .language:       OpenCL C
    .language_version:
      - 2
      - 0
    .max_flat_workgroup_size: 512
    .name:           _Z11gram_kernelPKfPKiS0_S0_S0_S0_S0_S0_S0_S0_S0_Pf
    .private_segment_fixed_size: 0
    .sgpr_count:     66
    .sgpr_spill_count: 0
    .symbol:         _Z11gram_kernelPKfPKiS0_S0_S0_S0_S0_S0_S0_S0_S0_Pf.kd
    .uniform_work_group_size: 1
    .uses_dynamic_stack: false
    .vgpr_count:     252
    .vgpr_spill_count: 0
    .wavefront_size: 64
  - .agpr_count:     0
    .args:
      - .actual_access:  read_only
        .address_space:  global
        .offset:         0
        .size:           8
        .value_kind:     global_buffer
      - .actual_access:  read_only
        .address_space:  global
        .offset:         8
        .size:           8
        .value_kind:     global_buffer
      - .actual_access:  write_only
        .address_space:  global
        .offset:         16
        .size:           8
        .value_kind:     global_buffer
    .group_segment_fixed_size: 0
    .kernarg_segment_align: 8
    .kernarg_segment_size: 24
    .language:       OpenCL C
    .language_version:
      - 2
      - 0
    .max_flat_workgroup_size: 256
    .name:           _Z10fin_kernelPKfS0_Pf
    .private_segment_fixed_size: 0
    .sgpr_count:     16
    .sgpr_spill_count: 0
    .symbol:         _Z10fin_kernelPKfS0_Pf.kd
    .uniform_work_group_size: 1
    .uses_dynamic_stack: false
    .vgpr_count:     50
    .vgpr_spill_count: 0
    .wavefront_size: 64
